# lean attention loop, waves 4-7 prioritised for the first 24 of every 64 fragments
# baseline (speedup 1.0000x reference)
.Lattn_pl0:
	s_waitcnt lgkmcnt(6)
	v_mfma_f32_16x16x32_bf16 v[64:67], v[160:163], v[96:99], 0
	v_exp_f32_e32 v88, v88
	v_mfma_f32_16x16x32_bf16 v[68:71], v[160:163], v[112:115], 0
	v_exp_f32_e32 v92, v92
	ds_read_b128 v[160:163], v201 offset:20480
	s_add_u32 s16, s22, s10
	s_addc_u32 s17, s23, s11
	s_add_u32 s15, s22, s12
	s_addc_u32 s14, s23, s13
	s_add_u32 s8, s16, 0x3bc00200
	s_addc_u32 s9, s17, 0
	s_add_u32 s6, s15, 0x23a50000
	s_addc_u32 s7, s14, 0
	v_mfma_f32_16x16x32_bf16 v[0:3], v[164:167], v[216:219], v[0:3]
	v_cvt_pk_bf16_f32 v242, v80, v81
	v_mfma_f32_16x16x32_bf16 v[4:7], v[164:167], v[238:241], v[4:7]
	v_exp_f32_e32 v89, v89
	ds_read_b128 v[164:167], v209 offset:8192
	s_waitcnt vmcnt(4)
	ds_write_b128 v225, v[152:155] offset:49152
	s_waitcnt lgkmcnt(7)
	v_mfma_f32_16x16x32_bf16 v[68:71], v[168:171], v[116:119], v[68:71]
	v_exp_f32_e32 v93, v93
	v_mfma_f32_16x16x32_bf16 v[64:67], v[168:171], v[100:103], v[64:67]
	v_cvt_pk_bf16_f32 v243, v82, v83
	ds_read_b128 v[168:171], v202 offset:20480
	ds_write_b128 v226, v[156:159] offset:49152
	v_mfma_f32_16x16x32_bf16 v[12:15], v[172:175], v[238:241], v[12:15]
	v_exp_f32_e32 v90, v90
	v_mfma_f32_16x16x32_bf16 v[8:11], v[172:175], v[216:219], v[8:11]
	v_exp_f32_e32 v94, v94
	ds_read_b128 v[172:175], v209 offset:10240
	ds_write_b64 v227, v[132:133] offset:32768
	s_waitcnt lgkmcnt(9)
	v_mfma_f32_16x16x32_bf16 v[64:67], v[176:179], v[104:107], v[64:67]
	v_cvt_pk_bf16_f32 v204, v84, v85
	v_mfma_f32_16x16x32_bf16 v[68:71], v[176:179], v[120:123], v[68:71]
	v_exp_f32_e32 v91, v91
	ds_read_b128 v[176:179], v203 offset:20480
	ds_write_b64 v228, v[134:135] offset:32768
	v_mfma_f32_16x16x32_bf16 v[16:19], v[180:183], v[216:219], v[16:19]
	v_exp_f32_e32 v95, v95
	v_mfma_f32_16x16x32_bf16 v[20:23], v[180:183], v[238:241], v[20:23]
	v_cvt_pk_bf16_f32 v205, v86, v87
	v_add_f32_e32 v220, v220, v88
	ds_read_b128 v[180:183], v209 offset:12288
	ds_write_b64 v229, v[128:129] offset:32768
	s_waitcnt lgkmcnt(11)
	v_mfma_f32_16x16x32_bf16 v[68:71], v[230:233], v[124:127], v[68:71]
	v_add_f32_e32 v221, v221, v92
	v_add_f32_e32 v220, v220, v89
	v_mfma_f32_16x16x32_bf16 v[64:67], v[230:233], v[108:111], v[64:67]
	v_add_f32_e32 v221, v221, v93
	v_cvt_pk_bf16_f32 v244, v88, v89
	ds_read_b128 v[230:233], v246 offset:20480
	ds_write_b64 v184, v[130:131] offset:32768
	v_mfma_f32_16x16x32_bf16 v[28:31], v[234:237], v[238:241], v[28:31]
	v_cvt_pk_bf16_f32 v245, v90, v91
	v_cvt_pk_bf16_f32 v206, v92, v93
	v_mfma_f32_16x16x32_bf16 v[24:27], v[234:237], v[216:219], v[24:27]
	v_cvt_pk_bf16_f32 v207, v94, v95
	ds_read_b128 v[234:237], v209 offset:14336
	global_load_dwordx4 v[132:135], v198, s[8:9]
	s_waitcnt lgkmcnt(12)
	v_mfma_f32_16x16x32_bf16 v[72:75], v[160:163], v[96:99], 0
	v_add_f32_e32 v220, v220, v90
	v_add_f32_e32 v221, v221, v94
	v_mfma_f32_16x16x32_bf16 v[76:79], v[160:163], v[112:115], 0
	v_add_f32_e32 v220, v220, v91
	v_add_f32_e32 v221, v221, v95
	ds_read_b128 v[160:163], v201 offset:24576
	global_load_dwordx4 v[128:131], v199, s[8:9]
	v_mfma_f32_16x16x32_bf16 v[32:35], v[164:167], v[216:219], v[32:35]
	v_add_f32_e32 v194, v194, v220
	v_add_f32_e32 v195, v195, v221
	v_mfma_f32_16x16x32_bf16 v[36:39], v[164:167], v[238:241], v[36:39]
	v_exp_f32_e32 v64, v64
	ds_read_b128 v[164:167], v210 offset:0
	global_load_dwordx4 v[152:155], v196, s[6:7]
	s_waitcnt lgkmcnt(10)
	v_mfma_f32_16x16x32_bf16 v[76:79], v[168:171], v[116:119], v[76:79]
	v_exp_f32_e32 v68, v68
	v_mfma_f32_16x16x32_bf16 v[72:75], v[168:171], v[100:103], v[72:75]
	v_exp_f32_e32 v65, v65
	ds_read_b128 v[168:171], v202 offset:24576
	global_load_dwordx4 v[156:159], v197, s[6:7]
	v_mfma_f32_16x16x32_bf16 v[44:47], v[172:175], v[238:241], v[44:47]
	v_exp_f32_e32 v69, v69
	v_mfma_f32_16x16x32_bf16 v[40:43], v[172:175], v[216:219], v[40:43]
	v_exp_f32_e32 v66, v66
	ds_read_b128 v[172:175], v210 offset:2048
	s_waitcnt lgkmcnt(8)
	v_mfma_f32_16x16x32_bf16 v[72:75], v[176:179], v[104:107], v[72:75]
	v_exp_f32_e32 v70, v70
	v_mfma_f32_16x16x32_bf16 v[76:79], v[176:179], v[120:123], v[76:79]
	v_exp_f32_e32 v67, v67
	ds_read_b128 v[176:179], v203 offset:24576
	v_mfma_f32_16x16x32_bf16 v[48:51], v[180:183], v[216:219], v[48:51]
	v_exp_f32_e32 v71, v71
	v_mfma_f32_16x16x32_bf16 v[52:55], v[180:183], v[238:241], v[52:55]
	v_add_f32_e32 v220, v64, v65
	ds_read_b128 v[180:183], v210 offset:4096
	s_waitcnt lgkmcnt(6)
	v_mfma_f32_16x16x32_bf16 v[76:79], v[230:233], v[124:127], v[76:79]
	v_add_f32_e32 v221, v68, v69
	v_mfma_f32_16x16x32_bf16 v[72:75], v[230:233], v[108:111], v[72:75]
	v_add_f32_e32 v220, v220, v66
	ds_read_b128 v[230:233], v246 offset:24576
	v_mfma_f32_16x16x32_bf16 v[60:63], v[234:237], v[238:241], v[60:63]
	v_add_f32_e32 v221, v221, v70
	v_add_f32_e32 v220, v220, v67
	v_mfma_f32_16x16x32_bf16 v[56:59], v[234:237], v[216:219], v[56:59]
	v_add_f32_e32 v221, v221, v71
	ds_read_b128 v[234:237], v210 offset:6144
	s_waitcnt lgkmcnt(6)
	v_mfma_f32_16x16x32_bf16 v[80:83], v[160:163], v[96:99], 0
	v_exp_f32_e32 v72, v72
	v_mfma_f32_16x16x32_bf16 v[84:87], v[160:163], v[112:115], 0
	v_exp_f32_e32 v76, v76
	ds_read_b128 v[160:163], v201 offset:28672
	v_mfma_f32_16x16x32_bf16 v[0:3], v[164:167], v[242:245], v[0:3]
	v_exp_f32_e32 v73, v73
	v_mfma_f32_16x16x32_bf16 v[4:7], v[164:167], v[204:207], v[4:7]
	v_exp_f32_e32 v77, v77
	ds_read_b128 v[164:167], v210 offset:8192
	s_waitcnt lgkmcnt(6)
	v_mfma_f32_16x16x32_bf16 v[84:87], v[168:171], v[116:119], v[84:87]
	v_exp_f32_e32 v74, v74
	v_mfma_f32_16x16x32_bf16 v[80:83], v[168:171], v[100:103], v[80:83]
	v_exp_f32_e32 v78, v78
	ds_read_b128 v[168:171], v202 offset:28672
	v_mfma_f32_16x16x32_bf16 v[12:15], v[172:175], v[204:207], v[12:15]
	v_exp_f32_e32 v75, v75
	v_mfma_f32_16x16x32_bf16 v[8:11], v[172:175], v[242:245], v[8:11]
	v_exp_f32_e32 v79, v79
	ds_read_b128 v[172:175], v210 offset:10240
	s_waitcnt lgkmcnt(6)
	v_mfma_f32_16x16x32_bf16 v[80:83], v[176:179], v[104:107], v[80:83]
	v_add_f32_e32 v220, v220, v72
	v_add_f32_e32 v221, v221, v76
	v_mfma_f32_16x16x32_bf16 v[84:87], v[176:179], v[120:123], v[84:87]
	v_add_f32_e32 v220, v220, v73
	ds_read_b128 v[176:179], v203 offset:28672
	v_mfma_f32_16x16x32_bf16 v[16:19], v[180:183], v[242:245], v[16:19]
	v_add_f32_e32 v221, v221, v77
	v_add_f32_e32 v220, v220, v74
	v_mfma_f32_16x16x32_bf16 v[20:23], v[180:183], v[204:207], v[20:23]
	v_add_f32_e32 v221, v221, v78
	ds_read_b128 v[180:183], v210 offset:12288
	s_waitcnt lgkmcnt(6)
	v_mfma_f32_16x16x32_bf16 v[84:87], v[230:233], v[124:127], v[84:87]
	v_add_f32_e32 v220, v220, v75
	v_add_f32_e32 v221, v221, v79
	v_mfma_f32_16x16x32_bf16 v[80:83], v[230:233], v[108:111], v[80:83]
	v_cvt_pk_bf16_f32 v216, v64, v65
	ds_read_b128 v[230:233], v246 offset:28672
	v_mfma_f32_16x16x32_bf16 v[28:31], v[234:237], v[204:207], v[28:31]
	v_cvt_pk_bf16_f32 v217, v66, v67
	v_cvt_pk_bf16_f32 v238, v68, v69
	v_mfma_f32_16x16x32_bf16 v[24:27], v[234:237], v[242:245], v[24:27]
	v_cvt_pk_bf16_f32 v239, v70, v71
	ds_read_b128 v[234:237], v210 offset:14336
	s_setprio 0
	s_waitcnt lgkmcnt(6)
	v_mfma_f32_16x16x32_bf16 v[88:91], v[160:163], v[96:99], 0
	v_exp_f32_e32 v80, v80
	v_mfma_f32_16x16x32_bf16 v[92:95], v[160:163], v[112:115], 0
	v_exp_f32_e32 v84, v84
	ds_read_b128 v[160:163], v201 offset:32768
	v_mfma_f32_16x16x32_bf16 v[32:35], v[164:167], v[242:245], v[32:35]
	v_exp_f32_e32 v81, v81
	v_mfma_f32_16x16x32_bf16 v[36:39], v[164:167], v[204:207], v[36:39]
	v_exp_f32_e32 v85, v85
	ds_read_b128 v[164:167], v209 offset:16384
	s_waitcnt lgkmcnt(6)
	v_mfma_f32_16x16x32_bf16 v[92:95], v[168:171], v[116:119], v[92:95]
	v_exp_f32_e32 v82, v82
	v_mfma_f32_16x16x32_bf16 v[88:91], v[168:171], v[100:103], v[88:91]
	v_exp_f32_e32 v86, v86
	ds_read_b128 v[168:171], v202 offset:32768
	v_mfma_f32_16x16x32_bf16 v[44:47], v[172:175], v[204:207], v[44:47]
	v_exp_f32_e32 v83, v83
	v_mfma_f32_16x16x32_bf16 v[40:43], v[172:175], v[242:245], v[40:43]
	v_exp_f32_e32 v87, v87
	ds_read_b128 v[172:175], v209 offset:18432
	s_waitcnt lgkmcnt(6)
	v_mfma_f32_16x16x32_bf16 v[88:91], v[176:179], v[104:107], v[88:91]
	v_add_f32_e32 v220, v220, v80
	v_add_f32_e32 v221, v221, v84
	v_mfma_f32_16x16x32_bf16 v[92:95], v[176:179], v[120:123], v[92:95]
	v_add_f32_e32 v220, v220, v81
	ds_read_b128 v[176:179], v203 offset:32768
	v_mfma_f32_16x16x32_bf16 v[48:51], v[180:183], v[242:245], v[48:51]
	v_add_f32_e32 v221, v221, v85
	v_add_f32_e32 v220, v220, v82
	v_mfma_f32_16x16x32_bf16 v[52:55], v[180:183], v[204:207], v[52:55]
	v_add_f32_e32 v221, v221, v86
	ds_read_b128 v[180:183], v209 offset:20480
	s_waitcnt lgkmcnt(6)
	v_mfma_f32_16x16x32_bf16 v[92:95], v[230:233], v[124:127], v[92:95]
	v_add_f32_e32 v220, v220, v83
	v_add_f32_e32 v221, v221, v87
	v_mfma_f32_16x16x32_bf16 v[88:91], v[230:233], v[108:111], v[88:91]
	v_cvt_pk_bf16_f32 v218, v72, v73
	ds_read_b128 v[230:233], v246 offset:32768
	v_mfma_f32_16x16x32_bf16 v[60:63], v[234:237], v[204:207], v[60:63]
	v_cvt_pk_bf16_f32 v219, v74, v75
	v_cvt_pk_bf16_f32 v240, v76, v77
	v_mfma_f32_16x16x32_bf16 v[56:59], v[234:237], v[242:245], v[56:59]
	v_cvt_pk_bf16_f32 v241, v78, v79
	ds_read_b128 v[234:237], v209 offset:22528
	s_waitcnt lgkmcnt(6)
	v_mfma_f32_16x16x32_bf16 v[64:67], v[160:163], v[96:99], 0
	v_exp_f32_e32 v88, v88
	v_mfma_f32_16x16x32_bf16 v[68:71], v[160:163], v[112:115], 0
	v_exp_f32_e32 v92, v92
	ds_read_b128 v[160:163], v201 offset:36864
	s_add_u32 s8, s16, 0x3bc00280
	s_addc_u32 s9, s17, 0
	s_add_u32 s6, s15, 0x23a60000
	s_addc_u32 s7, s14, 0
	v_mfma_f32_16x16x32_bf16 v[0:3], v[164:167], v[216:219], v[0:3]
	v_cvt_pk_bf16_f32 v242, v80, v81
	v_mfma_f32_16x16x32_bf16 v[4:7], v[164:167], v[238:241], v[4:7]
	v_exp_f32_e32 v89, v89
	ds_read_b128 v[164:167], v209 offset:24576
	s_waitcnt vmcnt(4)
	ds_write_b128 v225, v[136:139] offset:0
	s_waitcnt lgkmcnt(7)
	v_mfma_f32_16x16x32_bf16 v[68:71], v[168:171], v[116:119], v[68:71]
	v_exp_f32_e32 v93, v93
	v_mfma_f32_16x16x32_bf16 v[64:67], v[168:171], v[100:103], v[64:67]
	v_cvt_pk_bf16_f32 v243, v82, v83
	ds_read_b128 v[168:171], v202 offset:36864
	ds_write_b128 v226, v[140:143] offset:0
	v_mfma_f32_16x16x32_bf16 v[12:15], v[172:175], v[238:241], v[12:15]
	v_exp_f32_e32 v90, v90
	v_mfma_f32_16x16x32_bf16 v[8:11], v[172:175], v[216:219], v[8:11]
	v_exp_f32_e32 v94, v94
	ds_read_b128 v[172:175], v209 offset:26624
	ds_write_b64 v227, v[148:149] offset:49152
	s_waitcnt lgkmcnt(9)
	v_mfma_f32_16x16x32_bf16 v[64:67], v[176:179], v[104:107], v[64:67]
	v_cvt_pk_bf16_f32 v204, v84, v85
	v_mfma_f32_16x16x32_bf16 v[68:71], v[176:179], v[120:123], v[68:71]
	v_exp_f32_e32 v91, v91
	ds_read_b128 v[176:179], v203 offset:36864
	ds_write_b64 v228, v[150:151] offset:49152
	v_mfma_f32_16x16x32_bf16 v[16:19], v[180:183], v[216:219], v[16:19]
	v_exp_f32_e32 v95, v95
	v_mfma_f32_16x16x32_bf16 v[20:23], v[180:183], v[238:241], v[20:23]
	v_cvt_pk_bf16_f32 v205, v86, v87
	v_add_f32_e32 v220, v220, v88
	ds_read_b128 v[180:183], v209 offset:28672
	ds_write_b64 v229, v[144:145] offset:49152
	s_waitcnt lgkmcnt(11)
	v_mfma_f32_16x16x32_bf16 v[68:71], v[230:233], v[124:127], v[68:71]
	v_add_f32_e32 v221, v221, v92
	v_add_f32_e32 v220, v220, v89
	v_mfma_f32_16x16x32_bf16 v[64:67], v[230:233], v[108:111], v[64:67]
	v_add_f32_e32 v221, v221, v93
	v_cvt_pk_bf16_f32 v244, v88, v89
	ds_read_b128 v[230:233], v246 offset:36864
	ds_write_b64 v184, v[146:147] offset:49152
	v_mfma_f32_16x16x32_bf16 v[28:31], v[234:237], v[238:241], v[28:31]
	v_cvt_pk_bf16_f32 v245, v90, v91
	v_cvt_pk_bf16_f32 v206, v92, v93
	v_mfma_f32_16x16x32_bf16 v[24:27], v[234:237], v[216:219], v[24:27]
	v_cvt_pk_bf16_f32 v207, v94, v95
	ds_read_b128 v[234:237], v209 offset:30720
	global_load_dwordx4 v[148:151], v198, s[8:9]
	s_waitcnt lgkmcnt(12)
	v_mfma_f32_16x16x32_bf16 v[72:75], v[160:163], v[96:99], 0
	v_add_f32_e32 v220, v220, v90
	v_add_f32_e32 v221, v221, v94
	v_mfma_f32_16x16x32_bf16 v[76:79], v[160:163], v[112:115], 0
	v_add_f32_e32 v220, v220, v91
	v_add_f32_e32 v221, v221, v95
	ds_read_b128 v[160:163], v201 offset:40960
	global_load_dwordx4 v[144:147], v199, s[8:9]
	v_mfma_f32_16x16x32_bf16 v[32:35], v[164:167], v[216:219], v[32:35]
	v_add_f32_e32 v194, v194, v220
	v_add_f32_e32 v195, v195, v221
	v_mfma_f32_16x16x32_bf16 v[36:39], v[164:167], v[238:241], v[36:39]
	v_exp_f32_e32 v64, v64
	ds_read_b128 v[164:167], v210 offset:16384
	global_load_dwordx4 v[136:139], v196, s[6:7]
	s_waitcnt lgkmcnt(10)
	v_mfma_f32_16x16x32_bf16 v[76:79], v[168:171], v[116:119], v[76:79]
	v_exp_f32_e32 v68, v68
	v_mfma_f32_16x16x32_bf16 v[72:75], v[168:171], v[100:103], v[72:75]
	v_exp_f32_e32 v65, v65
	ds_read_b128 v[168:171], v202 offset:40960
	global_load_dwordx4 v[140:143], v197, s[6:7]
	v_mfma_f32_16x16x32_bf16 v[44:47], v[172:175], v[238:241], v[44:47]
	v_exp_f32_e32 v69, v69
	v_mfma_f32_16x16x32_bf16 v[40:43], v[172:175], v[216:219], v[40:43]
	v_exp_f32_e32 v66, v66
	ds_read_b128 v[172:175], v210 offset:18432
	s_waitcnt lgkmcnt(8)
	v_mfma_f32_16x16x32_bf16 v[72:75], v[176:179], v[104:107], v[72:75]
	v_exp_f32_e32 v70, v70
	v_mfma_f32_16x16x32_bf16 v[76:79], v[176:179], v[120:123], v[76:79]
	v_exp_f32_e32 v67, v67
	ds_read_b128 v[176:179], v203 offset:40960
	v_mfma_f32_16x16x32_bf16 v[48:51], v[180:183], v[216:219], v[48:51]
	v_exp_f32_e32 v71, v71
	v_mfma_f32_16x16x32_bf16 v[52:55], v[180:183], v[238:241], v[52:55]
	v_add_f32_e32 v220, v64, v65
	ds_read_b128 v[180:183], v210 offset:20480
	s_waitcnt lgkmcnt(6)
	v_mfma_f32_16x16x32_bf16 v[76:79], v[230:233], v[124:127], v[76:79]
	v_add_f32_e32 v221, v68, v69
	v_mfma_f32_16x16x32_bf16 v[72:75], v[230:233], v[108:111], v[72:75]
	v_add_f32_e32 v220, v220, v66
	ds_read_b128 v[230:233], v246 offset:40960
	v_mfma_f32_16x16x32_bf16 v[60:63], v[234:237], v[238:241], v[60:63]
	v_add_f32_e32 v221, v221, v70
	v_add_f32_e32 v220, v220, v67
	v_mfma_f32_16x16x32_bf16 v[56:59], v[234:237], v[216:219], v[56:59]
	v_add_f32_e32 v221, v221, v71
	ds_read_b128 v[234:237], v210 offset:22528
	s_waitcnt lgkmcnt(6)
	v_mfma_f32_16x16x32_bf16 v[80:83], v[160:163], v[96:99], 0
	v_exp_f32_e32 v72, v72
	v_mfma_f32_16x16x32_bf16 v[84:87], v[160:163], v[112:115], 0
	v_exp_f32_e32 v76, v76
	ds_read_b128 v[160:163], v201 offset:45056
	v_mfma_f32_16x16x32_bf16 v[0:3], v[164:167], v[242:245], v[0:3]
	v_exp_f32_e32 v73, v73
	v_mfma_f32_16x16x32_bf16 v[4:7], v[164:167], v[204:207], v[4:7]
	v_exp_f32_e32 v77, v77
	ds_read_b128 v[164:167], v210 offset:24576
	s_waitcnt lgkmcnt(6)
	v_mfma_f32_16x16x32_bf16 v[84:87], v[168:171], v[116:119], v[84:87]
	v_exp_f32_e32 v74, v74
	v_mfma_f32_16x16x32_bf16 v[80:83], v[168:171], v[100:103], v[80:83]
	v_exp_f32_e32 v78, v78
	ds_read_b128 v[168:171], v202 offset:45056
	v_mfma_f32_16x16x32_bf16 v[12:15], v[172:175], v[204:207], v[12:15]
	v_exp_f32_e32 v75, v75
	v_mfma_f32_16x16x32_bf16 v[8:11], v[172:175], v[242:245], v[8:11]
	v_exp_f32_e32 v79, v79
	ds_read_b128 v[172:175], v210 offset:26624
	s_waitcnt lgkmcnt(6)
	v_mfma_f32_16x16x32_bf16 v[80:83], v[176:179], v[104:107], v[80:83]
	v_add_f32_e32 v220, v220, v72
	v_add_f32_e32 v221, v221, v76
	v_mfma_f32_16x16x32_bf16 v[84:87], v[176:179], v[120:123], v[84:87]
	v_add_f32_e32 v220, v220, v73
	ds_read_b128 v[176:179], v203 offset:45056
	v_mfma_f32_16x16x32_bf16 v[16:19], v[180:183], v[242:245], v[16:19]
	v_add_f32_e32 v221, v221, v77
	v_add_f32_e32 v220, v220, v74
	v_mfma_f32_16x16x32_bf16 v[20:23], v[180:183], v[204:207], v[20:23]
	v_add_f32_e32 v221, v221, v78
	ds_read_b128 v[180:183], v210 offset:28672
	s_waitcnt lgkmcnt(6)
	v_mfma_f32_16x16x32_bf16 v[84:87], v[230:233], v[124:127], v[84:87]
	v_add_f32_e32 v220, v220, v75
	v_add_f32_e32 v221, v221, v79
	v_mfma_f32_16x16x32_bf16 v[80:83], v[230:233], v[108:111], v[80:83]
	v_cvt_pk_bf16_f32 v216, v64, v65
	ds_read_b128 v[230:233], v246 offset:45056
	v_mfma_f32_16x16x32_bf16 v[28:31], v[234:237], v[204:207], v[28:31]
	v_cvt_pk_bf16_f32 v217, v66, v67
	v_cvt_pk_bf16_f32 v238, v68, v69
	v_mfma_f32_16x16x32_bf16 v[24:27], v[234:237], v[242:245], v[24:27]
	v_cvt_pk_bf16_f32 v239, v70, v71
	ds_read_b128 v[234:237], v210 offset:30720
	s_waitcnt lgkmcnt(6)
	v_mfma_f32_16x16x32_bf16 v[88:91], v[160:163], v[96:99], 0
	v_exp_f32_e32 v80, v80
	v_mfma_f32_16x16x32_bf16 v[92:95], v[160:163], v[112:115], 0
	v_exp_f32_e32 v84, v84
	v_mfma_f32_16x16x32_bf16 v[32:35], v[164:167], v[242:245], v[32:35]
	v_exp_f32_e32 v81, v81
	v_mfma_f32_16x16x32_bf16 v[36:39], v[164:167], v[204:207], v[36:39]
	v_exp_f32_e32 v85, v85
	s_waitcnt lgkmcnt(4)
	v_mfma_f32_16x16x32_bf16 v[92:95], v[168:171], v[116:119], v[92:95]
	v_exp_f32_e32 v82, v82
	v_mfma_f32_16x16x32_bf16 v[88:91], v[168:171], v[100:103], v[88:91]
	v_exp_f32_e32 v86, v86
	v_mfma_f32_16x16x32_bf16 v[44:47], v[172:175], v[204:207], v[44:47]
	v_exp_f32_e32 v83, v83
	v_mfma_f32_16x16x32_bf16 v[40:43], v[172:175], v[242:245], v[40:43]
	v_exp_f32_e32 v87, v87
	s_waitcnt lgkmcnt(3)
	v_mfma_f32_16x16x32_bf16 v[88:91], v[176:179], v[104:107], v[88:91]
	v_add_f32_e32 v220, v220, v80
	v_add_f32_e32 v221, v221, v84
	v_mfma_f32_16x16x32_bf16 v[92:95], v[176:179], v[120:123], v[92:95]
	v_add_f32_e32 v220, v220, v81
	s_waitcnt lgkmcnt(0)
	s_barrier
	ds_read_b128 v[160:163], v201 offset:49152
	ds_read_b128 v[164:167], v209 offset:32768
	ds_read_b128 v[168:171], v202 offset:49152
	ds_read_b128 v[172:175], v209 offset:34816
	ds_read_b128 v[176:179], v203 offset:49152
	v_mfma_f32_16x16x32_bf16 v[48:51], v[180:183], v[242:245], v[48:51]
	v_add_f32_e32 v221, v221, v85
	v_add_f32_e32 v220, v220, v82
	v_mfma_f32_16x16x32_bf16 v[52:55], v[180:183], v[204:207], v[52:55]
	v_add_f32_e32 v221, v221, v86
	ds_read_b128 v[180:183], v209 offset:36864
	v_mfma_f32_16x16x32_bf16 v[92:95], v[230:233], v[124:127], v[92:95]
	v_add_f32_e32 v220, v220, v83
	v_add_f32_e32 v221, v221, v87
	v_mfma_f32_16x16x32_bf16 v[88:91], v[230:233], v[108:111], v[88:91]
	v_cvt_pk_bf16_f32 v218, v72, v73
	ds_read_b128 v[230:233], v246 offset:49152
	v_mfma_f32_16x16x32_bf16 v[60:63], v[234:237], v[204:207], v[60:63]
	v_cvt_pk_bf16_f32 v219, v74, v75
	v_cvt_pk_bf16_f32 v240, v76, v77
	v_mfma_f32_16x16x32_bf16 v[56:59], v[234:237], v[242:245], v[56:59]
	v_cvt_pk_bf16_f32 v241, v78, v79
	ds_read_b128 v[234:237], v209 offset:38912
	s_cmp_eq_u32 s100, 0
	s_cbranch_scc1 .Lattn_pl64
	s_setprio 1
.Lattn_pl64:
	s_waitcnt lgkmcnt(6)
	v_mfma_f32_16x16x32_bf16 v[64:67], v[160:163], v[96:99], 0
	v_exp_f32_e32 v88, v88
	v_mfma_f32_16x16x32_bf16 v[68:71], v[160:163], v[112:115], 0
	v_exp_f32_e32 v92, v92
	ds_read_b128 v[160:163], v201 offset:53248
	s_add_u32 s8, s16, 0x3bc00300
	s_addc_u32 s9, s17, 0
	s_add_u32 s6, s15, 0x23a70000
	s_addc_u32 s7, s14, 0
	v_mfma_f32_16x16x32_bf16 v[0:3], v[164:167], v[216:219], v[0:3]
	v_cvt_pk_bf16_f32 v242, v80, v81
	v_mfma_f32_16x16x32_bf16 v[4:7], v[164:167], v[238:241], v[4:7]
	v_exp_f32_e32 v89, v89
	ds_read_b128 v[164:167], v209 offset:40960
	s_waitcnt vmcnt(4)
	ds_write_b128 v225, v[152:155] offset:16384
	s_waitcnt lgkmcnt(7)
	v_mfma_f32_16x16x32_bf16 v[68:71], v[168:171], v[116:119], v[68:71]
	v_exp_f32_e32 v93, v93
	v_mfma_f32_16x16x32_bf16 v[64:67], v[168:171], v[100:103], v[64:67]
	v_cvt_pk_bf16_f32 v243, v82, v83
	ds_read_b128 v[168:171], v202 offset:53248
	ds_write_b128 v226, v[156:159] offset:16384
	v_mfma_f32_16x16x32_bf16 v[12:15], v[172:175], v[238:241], v[12:15]
	v_exp_f32_e32 v90, v90
	v_mfma_f32_16x16x32_bf16 v[8:11], v[172:175], v[216:219], v[8:11]
	v_exp_f32_e32 v94, v94
	ds_read_b128 v[172:175], v209 offset:43008
	ds_write_b64 v227, v[132:133] offset:0
	s_waitcnt lgkmcnt(9)
	v_mfma_f32_16x16x32_bf16 v[64:67], v[176:179], v[104:107], v[64:67]
	v_cvt_pk_bf16_f32 v204, v84, v85
	v_mfma_f32_16x16x32_bf16 v[68:71], v[176:179], v[120:123], v[68:71]
	v_exp_f32_e32 v91, v91
	ds_read_b128 v[176:179], v203 offset:53248
	ds_write_b64 v228, v[134:135] offset:0
	v_mfma_f32_16x16x32_bf16 v[16:19], v[180:183], v[216:219], v[16:19]
	v_exp_f32_e32 v95, v95
	v_mfma_f32_16x16x32_bf16 v[20:23], v[180:183], v[238:241], v[20:23]
	v_cvt_pk_bf16_f32 v205, v86, v87
	v_add_f32_e32 v220, v220, v88
	ds_read_b128 v[180:183], v209 offset:45056
	ds_write_b64 v229, v[128:129] offset:0
	s_waitcnt lgkmcnt(11)
	v_mfma_f32_16x16x32_bf16 v[68:71], v[230:233], v[124:127], v[68:71]
	v_add_f32_e32 v221, v221, v92
	v_add_f32_e32 v220, v220, v89
	v_mfma_f32_16x16x32_bf16 v[64:67], v[230:233], v[108:111], v[64:67]
	v_add_f32_e32 v221, v221, v93
	v_cvt_pk_bf16_f32 v244, v88, v89
	ds_read_b128 v[230:233], v246 offset:53248
	ds_write_b64 v184, v[130:131] offset:0
	v_mfma_f32_16x16x32_bf16 v[28:31], v[234:237], v[238:241], v[28:31]
	v_cvt_pk_bf16_f32 v245, v90, v91
	v_cvt_pk_bf16_f32 v206, v92, v93
	v_mfma_f32_16x16x32_bf16 v[24:27], v[234:237], v[216:219], v[24:27]
	v_cvt_pk_bf16_f32 v207, v94, v95
	ds_read_b128 v[234:237], v209 offset:47104
	global_load_dwordx4 v[132:135], v198, s[8:9]
	s_waitcnt lgkmcnt(12)
	v_mfma_f32_16x16x32_bf16 v[72:75], v[160:163], v[96:99], 0
	v_add_f32_e32 v220, v220, v90
	v_add_f32_e32 v221, v221, v94
	v_mfma_f32_16x16x32_bf16 v[76:79], v[160:163], v[112:115], 0
	v_add_f32_e32 v220, v220, v91
	v_add_f32_e32 v221, v221, v95
	ds_read_b128 v[160:163], v201 offset:57344
	global_load_dwordx4 v[128:131], v199, s[8:9]
	v_mfma_f32_16x16x32_bf16 v[32:35], v[164:167], v[216:219], v[32:35]
	v_add_f32_e32 v194, v194, v220
	v_add_f32_e32 v195, v195, v221
	v_mfma_f32_16x16x32_bf16 v[36:39], v[164:167], v[238:241], v[36:39]
	v_exp_f32_e32 v64, v64
	ds_read_b128 v[164:167], v210 offset:32768
	global_load_dwordx4 v[152:155], v196, s[6:7]
	s_waitcnt lgkmcnt(10)
	v_mfma_f32_16x16x32_bf16 v[76:79], v[168:171], v[116:119], v[76:79]
	v_exp_f32_e32 v68, v68
	v_mfma_f32_16x16x32_bf16 v[72:75], v[168:171], v[100:103], v[72:75]
	v_exp_f32_e32 v65, v65
	ds_read_b128 v[168:171], v202 offset:57344
	global_load_dwordx4 v[156:159], v197, s[6:7]
	v_mfma_f32_16x16x32_bf16 v[44:47], v[172:175], v[238:241], v[44:47]
	v_exp_f32_e32 v69, v69
	v_mfma_f32_16x16x32_bf16 v[40:43], v[172:175], v[216:219], v[40:43]
	v_exp_f32_e32 v66, v66
	ds_read_b128 v[172:175], v210 offset:34816
	s_waitcnt lgkmcnt(8)
	v_mfma_f32_16x16x32_bf16 v[72:75], v[176:179], v[104:107], v[72:75]
	v_exp_f32_e32 v70, v70
	v_mfma_f32_16x16x32_bf16 v[76:79], v[176:179], v[120:123], v[76:79]
	v_exp_f32_e32 v67, v67
	ds_read_b128 v[176:179], v203 offset:57344
	v_mfma_f32_16x16x32_bf16 v[48:51], v[180:183], v[216:219], v[48:51]
	v_exp_f32_e32 v71, v71
	v_mfma_f32_16x16x32_bf16 v[52:55], v[180:183], v[238:241], v[52:55]
	v_add_f32_e32 v220, v64, v65
	ds_read_b128 v[180:183], v210 offset:36864
	s_waitcnt lgkmcnt(6)
	v_mfma_f32_16x16x32_bf16 v[76:79], v[230:233], v[124:127], v[76:79]
	v_add_f32_e32 v221, v68, v69
	v_mfma_f32_16x16x32_bf16 v[72:75], v[230:233], v[108:111], v[72:75]
	v_add_f32_e32 v220, v220, v66
	ds_read_b128 v[230:233], v246 offset:57344
	v_mfma_f32_16x16x32_bf16 v[60:63], v[234:237], v[238:241], v[60:63]
	v_add_f32_e32 v221, v221, v70
	v_add_f32_e32 v220, v220, v67
	v_mfma_f32_16x16x32_bf16 v[56:59], v[234:237], v[216:219], v[56:59]
	v_add_f32_e32 v221, v221, v71
	ds_read_b128 v[234:237], v210 offset:38912
	s_waitcnt lgkmcnt(6)
	v_mfma_f32_16x16x32_bf16 v[80:83], v[160:163], v[96:99], 0
	v_exp_f32_e32 v72, v72
	v_mfma_f32_16x16x32_bf16 v[84:87], v[160:163], v[112:115], 0
	v_exp_f32_e32 v76, v76
	ds_read_b128 v[160:163], v201 offset:61440
	v_mfma_f32_16x16x32_bf16 v[0:3], v[164:167], v[242:245], v[0:3]
	v_exp_f32_e32 v73, v73
	v_mfma_f32_16x16x32_bf16 v[4:7], v[164:167], v[204:207], v[4:7]
	v_exp_f32_e32 v77, v77
	ds_read_b128 v[164:167], v210 offset:40960
	s_waitcnt lgkmcnt(6)
	v_mfma_f32_16x16x32_bf16 v[84:87], v[168:171], v[116:119], v[84:87]
	v_exp_f32_e32 v74, v74
	v_mfma_f32_16x16x32_bf16 v[80:83], v[168:171], v[100:103], v[80:83]
	v_exp_f32_e32 v78, v78
	ds_read_b128 v[168:171], v202 offset:61440
	v_mfma_f32_16x16x32_bf16 v[12:15], v[172:175], v[204:207], v[12:15]
	v_exp_f32_e32 v75, v75
	v_mfma_f32_16x16x32_bf16 v[8:11], v[172:175], v[242:245], v[8:11]
	v_exp_f32_e32 v79, v79
	ds_read_b128 v[172:175], v210 offset:43008
	s_waitcnt lgkmcnt(6)
	v_mfma_f32_16x16x32_bf16 v[80:83], v[176:179], v[104:107], v[80:83]
	v_add_f32_e32 v220, v220, v72
	v_add_f32_e32 v221, v221, v76
	v_mfma_f32_16x16x32_bf16 v[84:87], v[176:179], v[120:123], v[84:87]
	v_add_f32_e32 v220, v220, v73
	ds_read_b128 v[176:179], v203 offset:61440
	v_mfma_f32_16x16x32_bf16 v[16:19], v[180:183], v[242:245], v[16:19]
	v_add_f32_e32 v221, v221, v77
	v_add_f32_e32 v220, v220, v74
	v_mfma_f32_16x16x32_bf16 v[20:23], v[180:183], v[204:207], v[20:23]
	v_add_f32_e32 v221, v221, v78
	ds_read_b128 v[180:183], v210 offset:45056
	s_waitcnt lgkmcnt(6)
	v_mfma_f32_16x16x32_bf16 v[84:87], v[230:233], v[124:127], v[84:87]
	v_add_f32_e32 v220, v220, v75
	v_add_f32_e32 v221, v221, v79
	v_mfma_f32_16x16x32_bf16 v[80:83], v[230:233], v[108:111], v[80:83]
	v_cvt_pk_bf16_f32 v216, v64, v65
	ds_read_b128 v[230:233], v246 offset:61440
	v_mfma_f32_16x16x32_bf16 v[28:31], v[234:237], v[204:207], v[28:31]
	v_cvt_pk_bf16_f32 v217, v66, v67
	v_cvt_pk_bf16_f32 v238, v68, v69
	v_mfma_f32_16x16x32_bf16 v[24:27], v[234:237], v[242:245], v[24:27]
	v_cvt_pk_bf16_f32 v239, v70, v71
	ds_read_b128 v[234:237], v210 offset:47104
	s_setprio 0
	s_waitcnt lgkmcnt(6)
	v_mfma_f32_16x16x32_bf16 v[88:91], v[160:163], v[96:99], 0
	v_exp_f32_e32 v80, v80
	v_mfma_f32_16x16x32_bf16 v[92:95], v[160:163], v[112:115], 0
	v_exp_f32_e32 v84, v84
	ds_read_b128 v[160:163], v201 offset:0
	v_mfma_f32_16x16x32_bf16 v[32:35], v[164:167], v[242:245], v[32:35]
	v_exp_f32_e32 v81, v81
	v_mfma_f32_16x16x32_bf16 v[36:39], v[164:167], v[204:207], v[36:39]
	v_exp_f32_e32 v85, v85
	ds_read_b128 v[164:167], v209 offset:49152
	s_waitcnt lgkmcnt(6)
	v_mfma_f32_16x16x32_bf16 v[92:95], v[168:171], v[116:119], v[92:95]
	v_exp_f32_e32 v82, v82
	v_mfma_f32_16x16x32_bf16 v[88:91], v[168:171], v[100:103], v[88:91]
	v_exp_f32_e32 v86, v86
	ds_read_b128 v[168:171], v202 offset:0
	v_mfma_f32_16x16x32_bf16 v[44:47], v[172:175], v[204:207], v[44:47]
	v_exp_f32_e32 v83, v83
	v_mfma_f32_16x16x32_bf16 v[40:43], v[172:175], v[242:245], v[40:43]
	v_exp_f32_e32 v87, v87
	ds_read_b128 v[172:175], v209 offset:51200
	s_waitcnt lgkmcnt(6)
	v_mfma_f32_16x16x32_bf16 v[88:91], v[176:179], v[104:107], v[88:91]
	v_add_f32_e32 v220, v220, v80
	v_add_f32_e32 v221, v221, v84
	v_mfma_f32_16x16x32_bf16 v[92:95], v[176:179], v[120:123], v[92:95]
	v_add_f32_e32 v220, v220, v81
	ds_read_b128 v[176:179], v203 offset:0
	v_mfma_f32_16x16x32_bf16 v[48:51], v[180:183], v[242:245], v[48:51]
	v_add_f32_e32 v221, v221, v85
	v_add_f32_e32 v220, v220, v82
	v_mfma_f32_16x16x32_bf16 v[52:55], v[180:183], v[204:207], v[52:55]
	v_add_f32_e32 v221, v221, v86
	ds_read_b128 v[180:183], v209 offset:53248
	s_waitcnt lgkmcnt(6)
	v_mfma_f32_16x16x32_bf16 v[92:95], v[230:233], v[124:127], v[92:95]
	v_add_f32_e32 v220, v220, v83
	v_add_f32_e32 v221, v221, v87
	v_mfma_f32_16x16x32_bf16 v[88:91], v[230:233], v[108:111], v[88:91]
	v_cvt_pk_bf16_f32 v218, v72, v73
	ds_read_b128 v[230:233], v246 offset:0
	v_mfma_f32_16x16x32_bf16 v[60:63], v[234:237], v[204:207], v[60:63]
	v_cvt_pk_bf16_f32 v219, v74, v75
	v_cvt_pk_bf16_f32 v240, v76, v77
	v_mfma_f32_16x16x32_bf16 v[56:59], v[234:237], v[242:245], v[56:59]
	v_cvt_pk_bf16_f32 v241, v78, v79
	ds_read_b128 v[234:237], v209 offset:55296
	s_waitcnt lgkmcnt(6)
	v_mfma_f32_16x16x32_bf16 v[64:67], v[160:163], v[96:99], 0
	v_exp_f32_e32 v88, v88
	v_mfma_f32_16x16x32_bf16 v[68:71], v[160:163], v[112:115], 0
	v_exp_f32_e32 v92, v92
	ds_read_b128 v[160:163], v201 offset:4096
	s_add_u32 s8, s16, 0x3bc00380
	s_addc_u32 s9, s17, 0
	s_add_u32 s6, s15, 0x23a80000
	s_addc_u32 s7, s14, 0
	v_mfma_f32_16x16x32_bf16 v[0:3], v[164:167], v[216:219], v[0:3]
	v_cvt_pk_bf16_f32 v242, v80, v81
	v_mfma_f32_16x16x32_bf16 v[4:7], v[164:167], v[238:241], v[4:7]
	v_exp_f32_e32 v89, v89
	ds_read_b128 v[164:167], v209 offset:57344
	s_waitcnt vmcnt(4)
	ds_write_b128 v225, v[136:139] offset:32768
	s_waitcnt lgkmcnt(7)
	v_mfma_f32_16x16x32_bf16 v[68:71], v[168:171], v[116:119], v[68:71]
	v_exp_f32_e32 v93, v93
	v_mfma_f32_16x16x32_bf16 v[64:67], v[168:171], v[100:103], v[64:67]
	v_cvt_pk_bf16_f32 v243, v82, v83
	ds_read_b128 v[168:171], v202 offset:4096
	ds_write_b128 v226, v[140:143] offset:32768
	v_mfma_f32_16x16x32_bf16 v[12:15], v[172:175], v[238:241], v[12:15]
	v_exp_f32_e32 v90, v90
	v_mfma_f32_16x16x32_bf16 v[8:11], v[172:175], v[216:219], v[8:11]
	v_exp_f32_e32 v94, v94
	ds_read_b128 v[172:175], v209 offset:59392
	ds_write_b64 v227, v[148:149] offset:16384
	s_waitcnt lgkmcnt(9)
	v_mfma_f32_16x16x32_bf16 v[64:67], v[176:179], v[104:107], v[64:67]
	v_cvt_pk_bf16_f32 v204, v84, v85
	v_mfma_f32_16x16x32_bf16 v[68:71], v[176:179], v[120:123], v[68:71]
	v_exp_f32_e32 v91, v91
	ds_read_b128 v[176:179], v203 offset:4096
	ds_write_b64 v228, v[150:151] offset:16384
	v_mfma_f32_16x16x32_bf16 v[16:19], v[180:183], v[216:219], v[16:19]
	v_exp_f32_e32 v95, v95
	v_mfma_f32_16x16x32_bf16 v[20:23], v[180:183], v[238:241], v[20:23]
	v_cvt_pk_bf16_f32 v205, v86, v87
	v_add_f32_e32 v220, v220, v88
	ds_read_b128 v[180:183], v209 offset:61440
	ds_write_b64 v229, v[144:145] offset:16384
	s_waitcnt lgkmcnt(11)
	v_mfma_f32_16x16x32_bf16 v[68:71], v[230:233], v[124:127], v[68:71]
	v_add_f32_e32 v221, v221, v92
	v_add_f32_e32 v220, v220, v89
	v_mfma_f32_16x16x32_bf16 v[64:67], v[230:233], v[108:111], v[64:67]
	v_add_f32_e32 v221, v221, v93
	v_cvt_pk_bf16_f32 v244, v88, v89
	ds_read_b128 v[230:233], v246 offset:4096
	ds_write_b64 v184, v[146:147] offset:16384
	v_mfma_f32_16x16x32_bf16 v[28:31], v[234:237], v[238:241], v[28:31]
	v_cvt_pk_bf16_f32 v245, v90, v91
	v_cvt_pk_bf16_f32 v206, v92, v93
	v_mfma_f32_16x16x32_bf16 v[24:27], v[234:237], v[216:219], v[24:27]
	v_cvt_pk_bf16_f32 v207, v94, v95
	ds_read_b128 v[234:237], v209 offset:63488
	global_load_dwordx4 v[148:151], v198, s[8:9]
	s_waitcnt lgkmcnt(12)
	v_mfma_f32_16x16x32_bf16 v[72:75], v[160:163], v[96:99], 0
	v_add_f32_e32 v220, v220, v90
	v_add_f32_e32 v221, v221, v94
	v_mfma_f32_16x16x32_bf16 v[76:79], v[160:163], v[112:115], 0
	v_add_f32_e32 v220, v220, v91
	v_add_f32_e32 v221, v221, v95
	ds_read_b128 v[160:163], v201 offset:8192
	global_load_dwordx4 v[144:147], v199, s[8:9]
	v_mfma_f32_16x16x32_bf16 v[32:35], v[164:167], v[216:219], v[32:35]
	v_add_f32_e32 v194, v194, v220
	v_add_f32_e32 v195, v195, v221
	v_mfma_f32_16x16x32_bf16 v[36:39], v[164:167], v[238:241], v[36:39]
	v_exp_f32_e32 v64, v64
	ds_read_b128 v[164:167], v210 offset:49152
	global_load_dwordx4 v[136:139], v196, s[6:7]
	s_waitcnt lgkmcnt(10)
	v_mfma_f32_16x16x32_bf16 v[76:79], v[168:171], v[116:119], v[76:79]
	v_exp_f32_e32 v68, v68
	v_mfma_f32_16x16x32_bf16 v[72:75], v[168:171], v[100:103], v[72:75]
	v_exp_f32_e32 v65, v65
	ds_read_b128 v[168:171], v202 offset:8192
	global_load_dwordx4 v[140:143], v197, s[6:7]
	v_mfma_f32_16x16x32_bf16 v[44:47], v[172:175], v[238:241], v[44:47]
	v_exp_f32_e32 v69, v69
	v_mfma_f32_16x16x32_bf16 v[40:43], v[172:175], v[216:219], v[40:43]
	v_exp_f32_e32 v66, v66
	ds_read_b128 v[172:175], v210 offset:51200
	s_waitcnt lgkmcnt(8)
	v_mfma_f32_16x16x32_bf16 v[72:75], v[176:179], v[104:107], v[72:75]
	v_exp_f32_e32 v70, v70
	v_mfma_f32_16x16x32_bf16 v[76:79], v[176:179], v[120:123], v[76:79]
	v_exp_f32_e32 v67, v67
	ds_read_b128 v[176:179], v203 offset:8192
	v_mfma_f32_16x16x32_bf16 v[48:51], v[180:183], v[216:219], v[48:51]
	v_exp_f32_e32 v71, v71
	v_mfma_f32_16x16x32_bf16 v[52:55], v[180:183], v[238:241], v[52:55]
	v_add_f32_e32 v220, v64, v65
	ds_read_b128 v[180:183], v210 offset:53248
	s_waitcnt lgkmcnt(6)
	v_mfma_f32_16x16x32_bf16 v[76:79], v[230:233], v[124:127], v[76:79]
	v_add_f32_e32 v221, v68, v69
	v_mfma_f32_16x16x32_bf16 v[72:75], v[230:233], v[108:111], v[72:75]
	v_add_f32_e32 v220, v220, v66
	ds_read_b128 v[230:233], v246 offset:8192
	v_mfma_f32_16x16x32_bf16 v[60:63], v[234:237], v[238:241], v[60:63]
	v_add_f32_e32 v221, v221, v70
	v_add_f32_e32 v220, v220, v67
	v_mfma_f32_16x16x32_bf16 v[56:59], v[234:237], v[216:219], v[56:59]
	v_add_f32_e32 v221, v221, v71
	ds_read_b128 v[234:237], v210 offset:55296
	s_waitcnt lgkmcnt(6)
	v_mfma_f32_16x16x32_bf16 v[80:83], v[160:163], v[96:99], 0
	v_exp_f32_e32 v72, v72
	v_mfma_f32_16x16x32_bf16 v[84:87], v[160:163], v[112:115], 0
	v_exp_f32_e32 v76, v76
	ds_read_b128 v[160:163], v201 offset:12288
	v_mfma_f32_16x16x32_bf16 v[0:3], v[164:167], v[242:245], v[0:3]
	v_exp_f32_e32 v73, v73
	v_mfma_f32_16x16x32_bf16 v[4:7], v[164:167], v[204:207], v[4:7]
	v_exp_f32_e32 v77, v77
	ds_read_b128 v[164:167], v210 offset:57344
	s_waitcnt lgkmcnt(6)
	v_mfma_f32_16x16x32_bf16 v[84:87], v[168:171], v[116:119], v[84:87]
	v_exp_f32_e32 v74, v74
	v_mfma_f32_16x16x32_bf16 v[80:83], v[168:171], v[100:103], v[80:83]
	v_exp_f32_e32 v78, v78
	ds_read_b128 v[168:171], v202 offset:12288
	v_mfma_f32_16x16x32_bf16 v[12:15], v[172:175], v[204:207], v[12:15]
	v_exp_f32_e32 v75, v75
	v_mfma_f32_16x16x32_bf16 v[8:11], v[172:175], v[242:245], v[8:11]
	v_exp_f32_e32 v79, v79
	ds_read_b128 v[172:175], v210 offset:59392
	s_waitcnt lgkmcnt(6)
	v_mfma_f32_16x16x32_bf16 v[80:83], v[176:179], v[104:107], v[80:83]
	v_add_f32_e32 v220, v220, v72
	v_add_f32_e32 v221, v221, v76
	v_mfma_f32_16x16x32_bf16 v[84:87], v[176:179], v[120:123], v[84:87]
	v_add_f32_e32 v220, v220, v73
	ds_read_b128 v[176:179], v203 offset:12288
	s_add_u32 s10, s10, 0x200
	s_addc_u32 s11, s11, 0
	s_add_u32 s12, s12, 0x40000
	s_addc_u32 s13, s13, 0
	s_add_i32 s4, s4, 4
	s_cmpk_lt_u32 s4, 0x104
	s_cselect_b64 s[6:7], -1, 0
	s_and_b64 s[6:7], s[0:1], s[6:7]
	s_and_b64 vcc, exec, s[6:7]
	v_mfma_f32_16x16x32_bf16 v[16:19], v[180:183], v[242:245], v[16:19]
	v_add_f32_e32 v221, v221, v77
	v_add_f32_e32 v220, v220, v74
	v_mfma_f32_16x16x32_bf16 v[20:23], v[180:183], v[204:207], v[20:23]
	v_add_f32_e32 v221, v221, v78
	ds_read_b128 v[180:183], v210 offset:61440
	s_waitcnt lgkmcnt(6)
	v_mfma_f32_16x16x32_bf16 v[84:87], v[230:233], v[124:127], v[84:87]
	v_add_f32_e32 v220, v220, v75
	v_add_f32_e32 v221, v221, v79
	v_mfma_f32_16x16x32_bf16 v[80:83], v[230:233], v[108:111], v[80:83]
	v_cvt_pk_bf16_f32 v216, v64, v65
	ds_read_b128 v[230:233], v246 offset:12288
	v_mfma_f32_16x16x32_bf16 v[28:31], v[234:237], v[204:207], v[28:31]
	v_cvt_pk_bf16_f32 v217, v66, v67
	v_cvt_pk_bf16_f32 v238, v68, v69
	v_mfma_f32_16x16x32_bf16 v[24:27], v[234:237], v[242:245], v[24:27]
	v_cvt_pk_bf16_f32 v239, v70, v71
	ds_read_b128 v[234:237], v210 offset:63488
	s_waitcnt lgkmcnt(6)
	v_mfma_f32_16x16x32_bf16 v[88:91], v[160:163], v[96:99], 0
	v_exp_f32_e32 v80, v80
	v_mfma_f32_16x16x32_bf16 v[92:95], v[160:163], v[112:115], 0
	v_exp_f32_e32 v84, v84
	v_mfma_f32_16x16x32_bf16 v[32:35], v[164:167], v[242:245], v[32:35]
	v_exp_f32_e32 v81, v81
	v_mfma_f32_16x16x32_bf16 v[36:39], v[164:167], v[204:207], v[36:39]
	v_exp_f32_e32 v85, v85
	s_waitcnt lgkmcnt(4)
	v_mfma_f32_16x16x32_bf16 v[92:95], v[168:171], v[116:119], v[92:95]
	v_exp_f32_e32 v82, v82
	v_mfma_f32_16x16x32_bf16 v[88:91], v[168:171], v[100:103], v[88:91]
	v_exp_f32_e32 v86, v86
	v_mfma_f32_16x16x32_bf16 v[44:47], v[172:175], v[204:207], v[44:47]
	v_exp_f32_e32 v83, v83
	v_mfma_f32_16x16x32_bf16 v[40:43], v[172:175], v[242:245], v[40:43]
	v_exp_f32_e32 v87, v87
	s_waitcnt lgkmcnt(3)
	v_mfma_f32_16x16x32_bf16 v[88:91], v[176:179], v[104:107], v[88:91]
	v_add_f32_e32 v220, v220, v80
	v_add_f32_e32 v221, v221, v84
	v_mfma_f32_16x16x32_bf16 v[92:95], v[176:179], v[120:123], v[92:95]
	v_add_f32_e32 v220, v220, v81
	s_waitcnt lgkmcnt(0)
	s_barrier
	ds_read_b128 v[160:163], v201 offset:16384
	ds_read_b128 v[164:167], v209 offset:0
	ds_read_b128 v[168:171], v202 offset:16384
	ds_read_b128 v[172:175], v209 offset:2048
	ds_read_b128 v[176:179], v203 offset:16384
	v_mfma_f32_16x16x32_bf16 v[48:51], v[180:183], v[242:245], v[48:51]
	v_add_f32_e32 v221, v221, v85
	v_add_f32_e32 v220, v220, v82
	v_mfma_f32_16x16x32_bf16 v[52:55], v[180:183], v[204:207], v[52:55]
	v_add_f32_e32 v221, v221, v86
	ds_read_b128 v[180:183], v209 offset:4096
	v_mfma_f32_16x16x32_bf16 v[92:95], v[230:233], v[124:127], v[92:95]
	v_add_f32_e32 v220, v220, v83
	v_add_f32_e32 v221, v221, v87
	v_mfma_f32_16x16x32_bf16 v[88:91], v[230:233], v[108:111], v[88:91]
	v_cvt_pk_bf16_f32 v218, v72, v73
	ds_read_b128 v[230:233], v246 offset:16384
	v_mfma_f32_16x16x32_bf16 v[60:63], v[234:237], v[204:207], v[60:63]
	v_cvt_pk_bf16_f32 v219, v74, v75
	v_cvt_pk_bf16_f32 v240, v76, v77
	v_mfma_f32_16x16x32_bf16 v[56:59], v[234:237], v[242:245], v[56:59]
	v_cvt_pk_bf16_f32 v241, v78, v79
	ds_read_b128 v[234:237], v209 offset:6144
	s_cbranch_vccnz .LBB0_734
	s_setprio 0
	s_waitcnt vmcnt(0)
	s_nop 7
	s_nop 7
	ds_swizzle_b32 v64, v194 offset:swizzle(SWAP,16)
	s_waitcnt lgkmcnt(0)
	v_add_f32_e32 v194, v194, v64
	v_mov_b32_e32 v65, v194
	s_nop 1
	v_permlane32_swap_b32_e32 v194, v65
	v_add_f32_e32 v194, v194, v65
	s_nop 0
	v_rcp_f32_e32 v66, v194
	ds_swizzle_b32 v64, v195 offset:swizzle(SWAP,16)
	s_waitcnt lgkmcnt(0)
	v_add_f32_e32 v195, v195, v64
	v_mov_b32_e32 v65, v195
	s_nop 1
	v_permlane32_swap_b32_e32 v195, v65
	v_add_f32_e32 v195, v195, v65
	s_nop 0
	v_rcp_f32_e32 v67, v195
	v_readlane_b32 s100, v250, 8
	v_mbcnt_lo_u32_b32 v68, -1, 0
	v_mbcnt_hi_u32_b32 v68, -1, v68
	v_and_b32_e32 v69, 15, v68
	v_lshrrev_b32_e32 v70, 4, v68
	s_lshr_b32 s101, s100, 1
	v_add_u32_e32 v69, s101, v69
	v_lshlrev_b32_e32 v69, 12, v69
	v_and_b32_e32 v71, 1, v70
	v_lshlrev_b32_e32 v71, 5, v71
	v_and_b32_e32 v70, 2, v70
	v_lshl_add_u32 v71, v70, 3, v71
	v_add_u32_e32 v70, v69, v71
	v_add_u32_e32 v71, 0x10000, v70
	v_mul_f32_e32 v0, v0, v66
	v_mul_f32_e32 v1, v1, v66
	v_mul_f32_e32 v2, v2, v66
	v_mul_f32_e32 v3, v3, v66
	v_mul_f32_e32 v8, v8, v66
	v_mul_f32_e32 v9, v9, v66
	v_mul_f32_e32 v10, v10, v66
	v_mul_f32_e32 v11, v11, v66
	v_cvt_pk_bf16_f32 v72, v0, v1
	v_cvt_pk_bf16_f32 v73, v2, v3
	v_cvt_pk_bf16_f32 v74, v8, v9
	v_cvt_pk_bf16_f32 v75, v10, v11
	s_nop 1
	v_permlane16_swap_b32_e32 v72, v74
	v_permlane16_swap_b32_e32 v73, v75
	s_nop 1
	global_store_dwordx4 v70, v[72:75], s[58:59] offset:0
	v_mul_f32_e32 v16, v16, v66
	v_mul_f32_e32 v17, v17, v66
	v_mul_f32_e32 v18, v18, v66
	v_mul_f32_e32 v19, v19, v66
	v_mul_f32_e32 v24, v24, v66
	v_mul_f32_e32 v25, v25, v66
	v_mul_f32_e32 v26, v26, v66
	v_mul_f32_e32 v27, v27, v66
	v_cvt_pk_bf16_f32 v76, v16, v17
	v_cvt_pk_bf16_f32 v77, v18, v19
	v_cvt_pk_bf16_f32 v78, v24, v25
	v_cvt_pk_bf16_f32 v79, v26, v27
	s_nop 1
	v_permlane16_swap_b32_e32 v76, v78
	v_permlane16_swap_b32_e32 v77, v79
	s_nop 1
	global_store_dwordx4 v70, v[76:79], s[58:59] offset:64
	v_mul_f32_e32 v32, v32, v66
	v_mul_f32_e32 v33, v33, v66
	v_mul_f32_e32 v34, v34, v66
	v_mul_f32_e32 v35, v35, v66
	v_mul_f32_e32 v40, v40, v66
	v_mul_f32_e32 v41, v41, v66
	v_mul_f32_e32 v42, v42, v66
	v_mul_f32_e32 v43, v43, v66
	v_cvt_pk_bf16_f32 v80, v32, v33
	v_cvt_pk_bf16_f32 v81, v34, v35
	v_cvt_pk_bf16_f32 v82, v40, v41
	v_cvt_pk_bf16_f32 v83, v42, v43
	s_nop 1
	v_permlane16_swap_b32_e32 v80, v82
	v_permlane16_swap_b32_e32 v81, v83
	s_nop 1
	global_store_dwordx4 v70, v[80:83], s[58:59] offset:128
	v_mul_f32_e32 v48, v48, v66
	v_mul_f32_e32 v49, v49, v66
	v_mul_f32_e32 v50, v50, v66
	v_mul_f32_e32 v51, v51, v66
	v_mul_f32_e32 v56, v56, v66
	v_mul_f32_e32 v57, v57, v66
	v_mul_f32_e32 v58, v58, v66
	v_mul_f32_e32 v59, v59, v66
	v_cvt_pk_bf16_f32 v84, v48, v49
	v_cvt_pk_bf16_f32 v85, v50, v51
	v_cvt_pk_bf16_f32 v86, v56, v57
	v_cvt_pk_bf16_f32 v87, v58, v59
	s_nop 1
	v_permlane16_swap_b32_e32 v84, v86
	v_permlane16_swap_b32_e32 v85, v87
	s_nop 1
	global_store_dwordx4 v70, v[84:87], s[58:59] offset:192
	v_mul_f32_e32 v4, v4, v67
	v_mul_f32_e32 v5, v5, v67
	v_mul_f32_e32 v6, v6, v67
	v_mul_f32_e32 v7, v7, v67
	v_mul_f32_e32 v12, v12, v67
	v_mul_f32_e32 v13, v13, v67
	v_mul_f32_e32 v14, v14, v67
	v_mul_f32_e32 v15, v15, v67
	v_cvt_pk_bf16_f32 v88, v4, v5
	v_cvt_pk_bf16_f32 v89, v6, v7
	v_cvt_pk_bf16_f32 v90, v12, v13
	v_cvt_pk_bf16_f32 v91, v14, v15
	s_nop 1
	v_permlane16_swap_b32_e32 v88, v90
	v_permlane16_swap_b32_e32 v89, v91
	s_nop 1
	global_store_dwordx4 v71, v[88:91], s[58:59] offset:0
	v_mul_f32_e32 v20, v20, v67
	v_mul_f32_e32 v21, v21, v67
	v_mul_f32_e32 v22, v22, v67
	v_mul_f32_e32 v23, v23, v67
	v_mul_f32_e32 v28, v28, v67
	v_mul_f32_e32 v29, v29, v67
	v_mul_f32_e32 v30, v30, v67
	v_mul_f32_e32 v31, v31, v67
	v_cvt_pk_bf16_f32 v92, v20, v21
	v_cvt_pk_bf16_f32 v93, v22, v23
	v_cvt_pk_bf16_f32 v94, v28, v29
	v_cvt_pk_bf16_f32 v95, v30, v31
	s_nop 1
	v_permlane16_swap_b32_e32 v92, v94
	v_permlane16_swap_b32_e32 v93, v95
	s_nop 1
	global_store_dwordx4 v71, v[92:95], s[58:59] offset:64
	v_mul_f32_e32 v36, v36, v67
	v_mul_f32_e32 v37, v37, v67
	v_mul_f32_e32 v38, v38, v67
	v_mul_f32_e32 v39, v39, v67
	v_mul_f32_e32 v44, v44, v67
	v_mul_f32_e32 v45, v45, v67
	v_mul_f32_e32 v46, v46, v67
	v_mul_f32_e32 v47, v47, v67
	v_cvt_pk_bf16_f32 v72, v36, v37
	v_cvt_pk_bf16_f32 v73, v38, v39
	v_cvt_pk_bf16_f32 v74, v44, v45
	v_cvt_pk_bf16_f32 v75, v46, v47
	s_nop 1
	v_permlane16_swap_b32_e32 v72, v74
	v_permlane16_swap_b32_e32 v73, v75
	s_nop 1
	global_store_dwordx4 v71, v[72:75], s[58:59] offset:128
	v_mul_f32_e32 v52, v52, v67
	v_mul_f32_e32 v53, v53, v67
	v_mul_f32_e32 v54, v54, v67
	v_mul_f32_e32 v55, v55, v67
	v_mul_f32_e32 v60, v60, v67
	v_mul_f32_e32 v61, v61, v67
	v_mul_f32_e32 v62, v62, v67
	v_mul_f32_e32 v63, v63, v67
	v_cvt_pk_bf16_f32 v76, v52, v53
	v_cvt_pk_bf16_f32 v77, v54, v55
	v_cvt_pk_bf16_f32 v78, v60, v61
	v_cvt_pk_bf16_f32 v79, v62, v63
	s_nop 1
	v_permlane16_swap_b32_e32 v76, v78
	v_permlane16_swap_b32_e32 v77, v79
	s_nop 1
	global_store_dwordx4 v71, v[76:79], s[58:59] offset:192
	s_barrier
